# speedup vs baseline: 1.0053x; 1.0053x over previous
_Z16sum_layer_kernelPKfS0_Pf:
	s_load_dwordx4 s[4:7], s[0:1], 0x0
	s_load_dwordx2 s[8:9], s[0:1], 0x10
	v_lshrrev_b32_e32 v42, 6, v0
	v_bfe_u32 v41, v0, 5, 1
	v_and_b32_e32 v40, 31, v0
	v_readfirstlane_b32 s23, v42
	v_and_b32_e32 v43, 7, v0
	v_bfe_u32 v44, v0, 3, 3
	s_lshl_b32 s3, s2, 12
	s_lshl_b32 s19, s2, 7
	s_lshl_b32 s23, s23, 12
	v_lshlrev_b32_e32 v1, 11, v41
	v_lshl_or_b32 v1, v40, 2, v1
	s_mov_b32 m0, s23
	v_lshrrev_b32_e32 v46, 1, v44
	v_xor_b32_e32 v46, v43, v46
	v_lshlrev_b32_e32 v46, 4, v46
	v_lshl_add_u32 v35, v44, 16, v46
	v_lshl_add_u32 v35, v42, 21, v35
	v_add_u32_e32 v35, s19, v35
	v_xor_b32_e32 v86, 64, v35
	s_mov_b32 s20, 0x7fc00
	s_mov_b32 s21, 0xff800
	s_mov_b32 s22, 0x17f400
	s_mov_b32 s14, 0x200000
	s_mov_b32 s15, 0x20000
	v_and_b32_e32 v45, 63, v0
	v_lshlrev_b32_e32 v37, 4, v45
	s_add_u32 s54, s23, 0x4000
	s_waitcnt lgkmcnt(0)
	s_mov_b32 s12, s6
	s_and_b32 s13, s7, 0xffff
	s_and_b32 s5, s5, 0xffff
	s_mov_b32 s6, 0x800000
	s_mov_b32 s7, s15
	s_mov_b32 m0, s54
	s_nop 0
	buffer_load_dwordx4 v37, s[12:15], s3 offen nt lds
	buffer_load_dwordx4 v37, s[12:15], s3 offen offset:1024 nt lds
	buffer_load_dwordx4 v37, s[12:15], s3 offen offset:2048 nt lds
	buffer_load_dwordx4 v37, s[12:15], s3 offen offset:3072 nt lds
	s_mov_b32 m0, s23
	s_nop 0
	buffer_load_dwordx4 v35, s[4:7], 0 offen sc1 nt lds
	buffer_load_dwordx4 v86, s[4:7], s20 offen offset:1024 sc1 nt lds
	buffer_load_dwordx4 v35, s[4:7], s21 offen offset:2048 sc1 nt lds
	buffer_load_dwordx4 v86, s[4:7], s22 offen offset:3072 sc1 nt lds
	v_and_b32_e32 v45, 63, v0
	v_lshlrev_b32_e32 v36, 2, v40
	v_lshl_add_u32 v36, v41, 18, v36
	v_lshl_add_u32 v36, v42, 21, v36
	v_add_u32_e32 v36, s19, v36
	v_bfe_u32 v47, v40, 1, 3
	v_lshlrev_b32_e32 v39, 2, v41
	v_xor_b32_e32 v39, v39, v47
	v_lshlrev_b32_e32 v39, 4, v39
	v_lshl_add_u32 v39, v40, 7, v39
	v_lshl_add_u32 v39, v42, 12, v39
	v_xor_b32_e32 v81, 16, v39
	v_xor_b32_e32 v82, 32, v39
	v_xor_b32_e32 v83, 48, v39
	v_cmp_gt_u32_e32 vcc, 32, v45
	v_mov_b32_e32 v34, 0xc1600000
	v_mov_b32_e32 v84, 0x3fb8aa3b
	v_mov_b32_e32 v85, 0x3f317218
	s_lshl_b32 s24, 1, 16
	s_lshl_b32 s25, 2, 16
	s_lshl_b32 s26, 3, 16
	s_lshl_b32 s27, 8, 16
	s_lshl_b32 s28, 9, 16
	s_lshl_b32 s29, 10, 16
	s_lshl_b32 s30, 11, 16
	s_lshl_b32 s31, 16, 16
	s_lshl_b32 s32, 17, 16
	s_lshl_b32 s33, 18, 16
	s_lshl_b32 s34, 19, 16
	s_lshl_b32 s35, 24, 16
	s_lshl_b32 s36, 25, 16
	s_lshl_b32 s37, 26, 16
	s_lshl_b32 s38, 27, 16
	s_and_b32 s9, s9, 0xffff
	s_mov_b32 s10, s6
	s_mov_b32 s11, s15
	v_lshl_add_u32 v38, v42, 12, v1
	v_add_u32_e32 v38, 0x4000, v38
	v_add_u32_e32 v87, 0x400, v38
	s_waitcnt vmcnt(4)
	ds_read2_b32 v[18:19], v38 offset0:0 offset1:32
	ds_read2_b32 v[20:21], v38 offset0:64 offset1:96
	ds_read2_b32 v[22:23], v38 offset0:128 offset1:160
	ds_read2_b32 v[24:25], v38 offset0:192 offset1:224
	ds_read2_b32 v[26:27], v87 offset0:0 offset1:32
	ds_read2_b32 v[28:29], v87 offset0:64 offset1:96
	ds_read2_b32 v[30:31], v87 offset0:128 offset1:160
	ds_read2_b32 v[32:33], v87 offset0:192 offset1:224
	s_waitcnt lgkmcnt(0)
	v_max3_f32 v48, v18, v19, v20
	v_max3_f32 v50, v21, v22, v23
	v_max3_f32 v48, v48, v24, v25
	v_max3_f32 v50, v50, v26, v27
	v_max3_f32 v48, v48, v28, v29
	v_max3_f32 v50, v50, v30, v31
	v_max3_f32 v48, v48, v32, v33
	v_max_f32_e32 v48, v48, v50
	v_mov_b32_e32 v50, v48
	s_nop 1
	v_permlane32_swap_b32_e32 v48, v50
	v_max_f32_e32 v48, v48, v50
	v_fmamk_f32 v48, v48, 0x3fb8aa3b, v34
	v_pk_fma_f32 v[18:19], v[18:19], v[84:85], v[48:49] op_sel_hi:[1,0,0] neg_lo:[0,0,1] neg_hi:[0,0,1]
	v_exp_f32_e32 v18, v18
	v_exp_f32_e32 v19, v19
	v_pk_fma_f32 v[20:21], v[20:21], v[84:85], v[48:49] op_sel_hi:[1,0,0] neg_lo:[0,0,1] neg_hi:[0,0,1]
	v_exp_f32_e32 v20, v20
	v_exp_f32_e32 v21, v21
	v_pk_fma_f32 v[22:23], v[22:23], v[84:85], v[48:49] op_sel_hi:[1,0,0] neg_lo:[0,0,1] neg_hi:[0,0,1]
	v_exp_f32_e32 v22, v22
	v_exp_f32_e32 v23, v23
	v_pk_fma_f32 v[24:25], v[24:25], v[84:85], v[48:49] op_sel_hi:[1,0,0] neg_lo:[0,0,1] neg_hi:[0,0,1]
	v_exp_f32_e32 v24, v24
	v_exp_f32_e32 v25, v25
	v_pk_fma_f32 v[26:27], v[26:27], v[84:85], v[48:49] op_sel_hi:[1,0,0] neg_lo:[0,0,1] neg_hi:[0,0,1]
	v_exp_f32_e32 v26, v26
	v_exp_f32_e32 v27, v27
	v_pk_fma_f32 v[28:29], v[28:29], v[84:85], v[48:49] op_sel_hi:[1,0,0] neg_lo:[0,0,1] neg_hi:[0,0,1]
	v_exp_f32_e32 v28, v28
	v_exp_f32_e32 v29, v29
	v_pk_fma_f32 v[30:31], v[30:31], v[84:85], v[48:49] op_sel_hi:[1,0,0] neg_lo:[0,0,1] neg_hi:[0,0,1]
	v_exp_f32_e32 v30, v30
	v_exp_f32_e32 v31, v31
	v_pk_fma_f32 v[32:33], v[32:33], v[84:85], v[48:49] op_sel_hi:[1,0,0] neg_lo:[0,0,1] neg_hi:[0,0,1]
	v_exp_f32_e32 v32, v32
	v_exp_f32_e32 v33, v33
	v_pk_add_f32 v[56:57], v[18:19], v[20:21]
	v_pk_add_f32 v[58:59], v[22:23], v[24:25]
	v_pk_add_f32 v[60:61], v[26:27], v[28:29]
	v_pk_add_f32 v[62:63], v[30:31], v[32:33]
	v_pk_add_f32 v[56:57], v[56:57], v[58:59]
	v_pk_add_f32 v[60:61], v[60:61], v[62:63]
	v_pk_add_f32 v[56:57], v[56:57], v[60:61]
	v_add_f32_e32 v50, v56, v57
	v_mov_b32_e32 v51, v50
	s_nop 1
	v_permlane32_swap_b32_e32 v50, v51
	v_add_f32_e32 v50, v50, v51
	v_log_f32_e32 v50, v50
	v_cvt_pk_f16_f32 v40, v18, v19
	v_cvt_pk_f16_f32 v41, v20, v21
	v_cvt_pk_f16_f32 v42, v22, v23
	v_cvt_pk_f16_f32 v43, v24, v25
	v_cvt_pk_f16_f32 v44, v26, v27
	v_cvt_pk_f16_f32 v45, v28, v29
	v_cvt_pk_f16_f32 v46, v30, v31
	v_cvt_pk_f16_f32 v47, v32, v33
	v_add_f32_e32 v50, 0x41600000, v50
	v_mul_f32_e32 v50, 0xbf317218, v50
	v_cndmask_b32_e64 v51, v50, 1.0, vcc
	s_waitcnt vmcnt(0)
	ds_read_b128 v[2:5], v39
	ds_read_b128 v[6:9], v81
	ds_read_b128 v[10:13], v82
	ds_read_b128 v[14:17], v83
	s_waitcnt lgkmcnt(2)
	v_max3_f32 v52, v2, v3, v4
	v_max3_f32 v53, v5, v6, v7
	v_max_f32_e32 v52, v52, v8
	v_max_f32_e32 v53, v53, v9
	s_waitcnt lgkmcnt(0)
	v_max3_f32 v52, v52, v10, v11
	v_max3_f32 v53, v53, v12, v13
	v_max3_f32 v52, v52, v14, v15
	v_max3_f32 v53, v53, v16, v17
	v_max_f32_e32 v52, v52, v53
	v_mov_b32_e32 v53, v52
	s_nop 1
	v_permlane32_swap_b32_e32 v52, v53
	v_max_f32_e32 v52, v52, v53
	v_cndmask_b32_e32 v54, 1.0, v52, vcc
	v_fmamk_f32 v48, v52, 0x3fb8aa3b, v34
	v_pk_fma_f32 v[2:3], v[2:3], v[84:85], v[48:49] op_sel_hi:[1,0,0] neg_lo:[0,0,1] neg_hi:[0,0,1]
	v_mfma_f32_32x32x2_f32 v[64:79], v54, v51, 0
	v_exp_f32_e32 v2, v2
	v_exp_f32_e32 v3, v3
	v_pk_fma_f32 v[4:5], v[4:5], v[84:85], v[48:49] op_sel_hi:[1,0,0] neg_lo:[0,0,1] neg_hi:[0,0,1]
	v_exp_f32_e32 v4, v4
	v_exp_f32_e32 v5, v5
	v_pk_fma_f32 v[6:7], v[6:7], v[84:85], v[48:49] op_sel_hi:[1,0,0] neg_lo:[0,0,1] neg_hi:[0,0,1]
	v_exp_f32_e32 v6, v6
	v_exp_f32_e32 v7, v7
	v_pk_fma_f32 v[8:9], v[8:9], v[84:85], v[48:49] op_sel_hi:[1,0,0] neg_lo:[0,0,1] neg_hi:[0,0,1]
	v_exp_f32_e32 v8, v8
	v_exp_f32_e32 v9, v9
	v_pk_fma_f32 v[10:11], v[10:11], v[84:85], v[48:49] op_sel_hi:[1,0,0] neg_lo:[0,0,1] neg_hi:[0,0,1]
	v_exp_f32_e32 v10, v10
	v_cvt_pk_f16_f32 v56, v2, v3
	v_cvt_pk_f16_f32 v57, v4, v5
	v_cvt_pk_f16_f32 v58, v6, v7
	v_cvt_pk_f16_f32 v59, v8, v9
	v_exp_f32_e32 v11, v11
	v_pk_fma_f32 v[12:13], v[12:13], v[84:85], v[48:49] op_sel_hi:[1,0,0] neg_lo:[0,0,1] neg_hi:[0,0,1]
	v_exp_f32_e32 v12, v12
	v_mfma_f32_32x32x16_f16 v[18:33], v[56:59], v[40:43], 0
	v_exp_f32_e32 v13, v13
	v_pk_fma_f32 v[14:15], v[14:15], v[84:85], v[48:49] op_sel_hi:[1,0,0] neg_lo:[0,0,1] neg_hi:[0,0,1]
	v_exp_f32_e32 v14, v14
	v_exp_f32_e32 v15, v15
	v_pk_fma_f32 v[16:17], v[16:17], v[84:85], v[48:49] op_sel_hi:[1,0,0] neg_lo:[0,0,1] neg_hi:[0,0,1]
	v_exp_f32_e32 v16, v16
	v_exp_f32_e32 v17, v17
	v_cvt_pk_f16_f32 v60, v10, v11
	v_cvt_pk_f16_f32 v61, v12, v13
	v_cvt_pk_f16_f32 v62, v14, v15
	v_cvt_pk_f16_f32 v63, v16, v17
	s_nop 1
	v_mfma_f32_32x32x16_f16 v[18:33], v[60:63], v[44:47], v[18:33]
	s_nop 11
	v_log_f32_e32 v18, v18
	v_log_f32_e32 v19, v19
	v_log_f32_e32 v20, v20
	v_log_f32_e32 v21, v21
	v_log_f32_e32 v22, v22
	v_log_f32_e32 v23, v23
	v_pk_fma_f32 v[64:65], v[18:19], v[84:85], v[64:65] op_sel:[0,1,0] op_sel_hi:[1,1,1]
	buffer_store_dword v64, v36, s[8:11], 0 offen
	buffer_store_dword v65, v36, s[8:11], s24 offen
	v_log_f32_e32 v24, v24
	v_log_f32_e32 v25, v25
	v_pk_fma_f32 v[66:67], v[20:21], v[84:85], v[66:67] op_sel:[0,1,0] op_sel_hi:[1,1,1]
	buffer_store_dword v66, v36, s[8:11], s25 offen
	buffer_store_dword v67, v36, s[8:11], s26 offen
	v_log_f32_e32 v26, v26
	v_log_f32_e32 v27, v27
	v_pk_fma_f32 v[68:69], v[22:23], v[84:85], v[68:69] op_sel:[0,1,0] op_sel_hi:[1,1,1]
	buffer_store_dword v68, v36, s[8:11], s27 offen
	buffer_store_dword v69, v36, s[8:11], s28 offen
	v_log_f32_e32 v28, v28
	v_log_f32_e32 v29, v29
	v_pk_fma_f32 v[70:71], v[24:25], v[84:85], v[70:71] op_sel:[0,1,0] op_sel_hi:[1,1,1]
	buffer_store_dword v70, v36, s[8:11], s29 offen
	buffer_store_dword v71, v36, s[8:11], s30 offen
	v_log_f32_e32 v30, v30
	v_log_f32_e32 v31, v31
	v_pk_fma_f32 v[72:73], v[26:27], v[84:85], v[72:73] op_sel:[0,1,0] op_sel_hi:[1,1,1]
	buffer_store_dword v72, v36, s[8:11], s31 offen
	buffer_store_dword v73, v36, s[8:11], s32 offen
	v_log_f32_e32 v32, v32
	v_log_f32_e32 v33, v33
	v_pk_fma_f32 v[74:75], v[28:29], v[84:85], v[74:75] op_sel:[0,1,0] op_sel_hi:[1,1,1]
	buffer_store_dword v74, v36, s[8:11], s33 offen
	buffer_store_dword v75, v36, s[8:11], s34 offen
	v_pk_fma_f32 v[76:77], v[30:31], v[84:85], v[76:77] op_sel:[0,1,0] op_sel_hi:[1,1,1]
	buffer_store_dword v76, v36, s[8:11], s35 offen
	buffer_store_dword v77, v36, s[8:11], s36 offen
	v_pk_fma_f32 v[78:79], v[32:33], v[84:85], v[78:79] op_sel:[0,1,0] op_sel_hi:[1,1,1]
	buffer_store_dword v78, v36, s[8:11], s37 offen
	buffer_store_dword v79, v36, s[8:11], s38 offen
	s_endpgm
